# lever 4: one static s_setprio 1 for waves 4-7 across mixer A (reset to 0 at its exit)
# speedup vs baseline: 1.0046x; 1.0046x over previous
; #define LAS __attribute__((address_space(3)))
; __device__ __forceinline__ void mixer_a_phase(const bf16* AQ, const bf16* AK, const bf16* AV  , bf16* O, float* ST, float* ML, const float* rel_bias, LAS unsigned char* lds, int G, int blk, int tid, int lane, int wave) {
;     LAS float* tab = (LAS float*)lds; LAS unsigned char* vst = lds + BAND_VST_OFF + wave * 8192;
;     constexpr float M_FAST = 127.0f;
;     int cur_h = -1;
;     for (int u = blk; u < 512; u += G) {
;         const int h = u & 7, v = u >> 3, b = v >> 4, a = v & 15;
;         if (h != cur_h) {
;             __syncthreads();
;             for (int idx = tid; idx < 3 * TA_LEN; idx += NWAVES * 64) { const int br = idx / TA_LEN, i = idx % TA_LEN - TA_OFF, dil = br == 0 ? 1 : (br == 1 ? 4 : 16);
;                 tab[idx] = (i >= 0 && i <= 128) ? (rel_bias[h * 32 + t5_bucket((i - 64) * dil)] * LOG2E + 64.0f) * KAPPA : -1.0f; }
;             __syncthreads(); cur_h = h;
;         }
;         const int i5 = lane & 31, hh = lane >> 5;
;         const size_t tb0 = (size_t)b * SEQ;
.LBB0_343:
	v_readlane_b32 s0, v254, 10
	v_readlane_b32 s4, v255, 17
	s_cmpk_gt_i32 s0, 0x1ff
	v_readlane_b32 s5, v255, 18
	s_cbranch_scc1 .LBB0_423
	v_readlane_b32 s0, v254, 0
	v_readlane_b32 s1, v254, 1
	s_add_u32 s12, s0, 0x29400000
	v_readlane_b32 s8, v254, 59
	s_addc_u32 s13, s1, 0
	s_lshl_b32 s0, s8, 14
	s_cmp_ge_u32 s8, 4
	s_cbranch_scc0 .Lprio_a
	s_setprio 1
.Lprio_a:
	v_bfe_u32 v6, v1, 5, 1
	v_lshlrev_b32_e32 v8, 5, v1
	s_add_i32 s0, s0, 0
	v_lshlrev_b32_e32 v7, 10, v6
	v_and_b32_e32 v8, 0x180, v8
	v_add3_u32 v192, s0, v7, v8
	v_and_b32_e32 v8, 19, v1
	v_lshrrev_b32_e32 v9, 1, v1
	v_bfe_u32 v5, v1, 4, 1
	v_and_or_b32 v8, v9, 4, v8
	v_bfe_u32 v196, v1, 3, 3
	v_and_b32_e32 v9, 15, v1
	v_lshl_add_u32 v194, v5, 5, v192
	v_cmp_eq_u32_e32 vcc, v9, v5
	v_bitop3_b32 v5, v196, v1, 7 bitop3:0x78
	v_lshl_add_u32 v198, v5, 4, s0
	v_bitop3_b32 v5, v8, v6, 7 bitop3:0x6c
	v_lshlrev_b32_e32 v200, 4, v5
	v_or_b32_e32 v5, 2, v6
	v_bitop3_b32 v5, v8, v5, 7 bitop3:0x6c
	v_lshlrev_b32_e32 v201, 4, v5
	v_or_b32_e32 v5, 4, v6
	v_bitop3_b32 v5, v8, v5, 7 bitop3:0x6c
	v_lshlrev_b32_e32 v7, 3, v1
	v_lshlrev_b32_e32 v202, 4, v5
	v_or_b32_e32 v5, 6, v6
	v_and_b32_e32 v193, 24, v7
	v_lshlrev_b32_e32 v7, 1, v1
	v_bitop3_b32 v5, v8, v5, 7 bitop3:0x6c
	v_and_b32_e32 v2, 63, v1
	v_and_or_b32 v7, v7, 8, v8
	v_lshlrev_b32_e32 v203, 4, v5
	v_and_b32_e32 v5, 16, v1
	v_lshlrev_b32_e32 v8, 2, v1
	v_cmp_gt_u32_e64 s[6:7], 32, v2
	v_and_or_b32 v2, v8, 12, v5
	s_movk_i32 s1, 0xf00
	v_mov_b32_e32 v3, 0
	v_lshl_add_u32 v195, v7, 7, s0
	v_and_b32_e32 v7, 7, v1
	v_lshlrev_b32_e32 v204, 1, v2
	v_and_b32_e32 v2, 32, v1
	v_cmp_gt_i32_e64 s[2:3], s1, v1
	v_and_b32_e32 v141, 31, v1
	s_lshl_b32 s1, s8, 5
	v_readlane_b32 s9, v254, 6
	v_lshlrev_b32_e32 v142, 3, v7
	v_lshlrev_b32_e32 v144, 4, v7
	v_lshlrev_b32_e32 v6, 1, v2
	v_mov_b32_e32 v7, v3
	v_readlane_b32 s10, v255, 21
	s_cmpk_lt_u32 s9, 0x400
	v_cmp_eq_u32_e64 s[4:5], 0, v5
	v_lshl_add_u64 v[146:147], s[92:93], 0, v[6:7]
	v_mul_i32_i24_e32 v5, -4, v141
	v_readlane_b32 s11, v255, 22
	v_lshlrev_b32_e32 v6, 2, v141
	s_cselect_b64 s[18:19], -1, 0
	v_add_u32_e32 v199, s0, v144
	v_lshl_add_u64 v[148:149], s[10:11], 0, v[2:3]
	v_sub_u32_e32 v6, v2, v6
	v_lshl_add_u32 v2, v5, 2, v2
	s_and_b32 s0, s8, 0x3fffffc
	v_subrev_u32_e32 v2, s0, v2
	s_bfe_u32 s38, s9, 0x20006
	v_add_u32_e32 v2, 0, v2
	v_add_u32_e32 v210, 0x1c00, v2
	v_lshl_or_b32 v2, v196, 2, s38
	v_or_b32_e32 v211, 0xffffffe0, v2
	v_or_b32_e32 v212, 0xffffffc0, v2
	v_or_b32_e32 v213, 0xffffffa0, v2
	v_or_b32_e32 v214, 0xffffff80, v2
	v_mbcnt_lo_u32_b32 v2, -1, 0
	v_lshrrev_b32_e32 v4, 2, v1
	v_mov_b32_e32 v10, 0x3f803f80
	v_add_u32_e32 v6, 0, v6
	v_mbcnt_hi_u32_b32 v2, -1, v2
	v_and_b32_e32 v4, 8, v4
	v_lshlrev_b32_e32 v143, 4, v141
	v_cndmask_b32_e32 v70, 0, v10, vcc
	v_add_u32_e32 v206, 0x800, v6
	v_or_b32_e32 v7, s1, v196
	v_add_u32_e32 v208, 0x3000, v6
	v_lshl_add_u32 v6, v196, 4, s8
	v_and_or_b32 v2, v2, 64, v9
	v_readlane_b32 s43, v254, 10
	s_mov_b32 s17, 0
	v_or_b32_e32 v138, s1, v141
	v_mov_b32_e32 v139, v3
	v_add_u32_e32 v140, s8, v143
	v_mov_b32_e32 v71, v70
	v_mov_b32_e32 v72, v70
	v_mov_b32_e32 v73, v70
	v_lshlrev_b32_e32 v197, 7, v196
	v_add_u32_e32 v205, 0, v8
	v_subrev_u32_e32 v207, 32, v7
	v_add_u32_e32 v209, 0xfffffe00, v6
	v_mov_b32_e32 v145, v3
	s_mov_b32 s45, -1
	v_mov_b32_e32 v215, 0x42800000
	v_lshlrev_b32_e32 v150, 1, v4
	s_mov_b32 s39, 0xda24260
	s_mov_b64 s[20:21], 0x20000
	s_mov_b32 s40, 0x42000000
	s_mov_b32 s41, 0xc3e00000
	v_lshlrev_b32_e32 v216, 2, v2
	v_mov_b32_e32 v217, 0x43e00000
	s_mov_b32 s42, s43
	s_branch .LBB0_346

; __device__ __forceinline__ void mixer_a_phase(const bf16* AQ, const bf16* AK, const bf16* AV  , bf16* O, float* ST, float* ML, const float* rel_bias, LAS unsigned char* lds, int G, int blk, int tid, int lane, int wave) {
;     ...
;     }
; }
.LBB0_422:
	s_setprio 0
	v_readlane_b32 s4, v255, 17
	v_readlane_b32 s5, v255, 18
